# v90 + grid barrier: L1 invalidate issued at arrival (before polling / with the leader's write-back) instead of after the release is observed
# speedup vs baseline: 1.0190x; 1.0155x over previous
.Lopt27_1:
.LBB0_73:
	s_or_b64 exec, exec, s[4:5]
	s_mov_b64 s[4:5], exec
	v_mbcnt_lo_u32_b32 v0, s4, 0
	v_mbcnt_hi_u32_b32 v0, s5, v0
	v_cmp_eq_u32_e32 vcc, 0, v0
	s_waitcnt vmcnt(0)
.LBB0_75:
	s_waitcnt vmcnt(0)

.Lopt27_2:
.LBB0_223:
	s_or_b64 exec, exec, s[4:5]
	s_mov_b64 s[4:5], exec
	v_mbcnt_lo_u32_b32 v0, s4, 0
	v_mbcnt_hi_u32_b32 v0, s5, v0
	v_cmp_eq_u32_e32 vcc, 0, v0
	s_waitcnt vmcnt(0)
.LBB0_225:
	s_waitcnt vmcnt(0)

.Lopt27_3:
.LBB0_318:
	s_or_b64 exec, exec, s[4:5]
	s_mov_b64 s[4:5], exec
	v_mbcnt_lo_u32_b32 v0, s4, 0
	v_mbcnt_hi_u32_b32 v0, s5, v0
	v_cmp_eq_u32_e32 vcc, 0, v0
	s_waitcnt vmcnt(0)
.LBB0_320:
	s_waitcnt vmcnt(0)

.Lopt27_4:
.LBB0_391:
	s_or_b64 exec, exec, s[4:5]
	s_mov_b64 s[4:5], exec
	v_mbcnt_lo_u32_b32 v0, s4, 0
	v_mbcnt_hi_u32_b32 v0, s5, v0
	v_cmp_eq_u32_e32 vcc, 0, v0
	s_waitcnt vmcnt(0)
.LBB0_393:
	s_waitcnt vmcnt(0)

.Lopt27_5:
.LBB0_516:
	s_or_b64 exec, exec, s[4:5]
	s_mov_b64 s[4:5], exec
	v_mbcnt_lo_u32_b32 v0, s4, 0
	v_mbcnt_hi_u32_b32 v0, s5, v0
	v_cmp_eq_u32_e32 vcc, 0, v0
	s_waitcnt vmcnt(0)
.LBB0_518:
	s_waitcnt vmcnt(0)

.Lopt27_6:
.LBB0_575:
	s_or_b64 exec, exec, s[4:5]
	s_mov_b64 s[4:5], exec
	v_mbcnt_lo_u32_b32 v0, s4, 0
	v_mbcnt_hi_u32_b32 v0, s5, v0
	v_cmp_eq_u32_e32 vcc, 0, v0
	s_waitcnt vmcnt(0)
.LBB0_577:
	s_waitcnt vmcnt(0)

.Lopt27_7:
.LBB0_716:
	s_or_b64 exec, exec, s[4:5]
	s_mov_b64 s[4:5], exec
	v_mbcnt_lo_u32_b32 v0, s4, 0
	v_mbcnt_hi_u32_b32 v0, s5, v0
	v_cmp_eq_u32_e32 vcc, 0, v0
	s_waitcnt vmcnt(0)
.LBB0_718:
	s_waitcnt vmcnt(0)

.Lopt27_8:
.LBB0_852:
	s_or_b64 exec, exec, s[4:5]
	s_mov_b64 s[4:5], exec
	v_mbcnt_lo_u32_b32 v0, s4, 0
	v_mbcnt_hi_u32_b32 v0, s5, v0
	v_cmp_eq_u32_e32 vcc, 0, v0
	s_waitcnt vmcnt(0)
.LBB0_854:
	s_waitcnt vmcnt(0)

.Lopt27_9:
.LBB0_967:
	s_or_b64 exec, exec, s[4:5]
	s_mov_b64 s[4:5], exec
	v_mbcnt_lo_u32_b32 v0, s4, 0
	v_mbcnt_hi_u32_b32 v0, s5, v0
	v_cmp_eq_u32_e32 vcc, 0, v0
	s_waitcnt vmcnt(0)
.LBB0_969:
	s_waitcnt vmcnt(0)

.Lopt27_10:
.LBB0_1063:
	s_or_b64 exec, exec, s[4:5]
	s_mov_b64 s[4:5], exec
	v_mbcnt_lo_u32_b32 v0, s4, 0
	v_mbcnt_hi_u32_b32 v0, s5, v0
	v_cmp_eq_u32_e32 vcc, 0, v0
	s_waitcnt vmcnt(0)
.LBB0_1065:
	s_waitcnt vmcnt(0)

.Lopt27_11:
.LBB0_1449:
	s_or_b64 exec, exec, s[4:5]
	s_mov_b64 s[4:5], exec
	v_mbcnt_lo_u32_b32 v0, s4, 0
	v_mbcnt_hi_u32_b32 v0, s5, v0
	v_cmp_eq_u32_e32 vcc, 0, v0
	s_waitcnt vmcnt(0)
.LBB0_1451:
	s_waitcnt vmcnt(0)

.Lopt27_12:
.LBB0_1636:
	s_or_b64 exec, exec, s[4:5]
	s_mov_b64 s[4:5], exec
	v_mbcnt_lo_u32_b32 v0, s4, 0
	v_mbcnt_hi_u32_b32 v0, s5, v0
	v_cmp_eq_u32_e32 vcc, 0, v0
	s_waitcnt vmcnt(0)
.LBB0_1638:
	s_waitcnt vmcnt(0)

.Lopt27_13:
.LBB0_1900:
	s_or_b64 exec, exec, s[4:5]
	s_mov_b64 s[4:5], exec
	v_mbcnt_lo_u32_b32 v0, s4, 0
	v_mbcnt_hi_u32_b32 v0, s5, v0
	v_cmp_eq_u32_e32 vcc, 0, v0
	s_waitcnt vmcnt(0)
.LBB0_1902:
	s_waitcnt vmcnt(0)

.Lopt27_14:
.LBB0_1973:
	s_or_b64 exec, exec, s[4:5]
	s_mov_b64 s[4:5], exec
	v_mbcnt_lo_u32_b32 v0, s4, 0
	v_mbcnt_hi_u32_b32 v0, s5, v0
	v_cmp_eq_u32_e32 vcc, 0, v0
	s_waitcnt vmcnt(0)
.LBB0_1975:
	s_waitcnt vmcnt(0)

.Lopt27_15:
.LBB0_2098:
	s_or_b64 exec, exec, s[4:5]
	s_mov_b64 s[4:5], exec
	v_mbcnt_lo_u32_b32 v0, s4, 0
	v_mbcnt_hi_u32_b32 v0, s5, v0
	v_cmp_eq_u32_e32 vcc, 0, v0
	s_waitcnt vmcnt(0)
.LBB0_2100:
	s_waitcnt vmcnt(0)

.Lopt27_16:
.LBB0_2157:
	s_or_b64 exec, exec, s[4:5]
	s_mov_b64 s[4:5], exec
	v_mbcnt_lo_u32_b32 v0, s4, 0
	v_mbcnt_hi_u32_b32 v0, s5, v0
	v_cmp_eq_u32_e32 vcc, 0, v0
	s_waitcnt vmcnt(0)
.LBB0_2159:
	s_waitcnt vmcnt(0)

.Lopt27_17:
.LBB0_2298:
	s_or_b64 exec, exec, s[4:5]
	s_mov_b64 s[4:5], exec
	v_mbcnt_lo_u32_b32 v0, s4, 0
	v_mbcnt_hi_u32_b32 v0, s5, v0
	v_cmp_eq_u32_e32 vcc, 0, v0
	s_waitcnt vmcnt(0)
.LBB0_2300:
	s_waitcnt vmcnt(0)

.Lopt27_18:
.LBB0_2432:
	s_or_b64 exec, exec, s[4:5]
	s_mov_b64 s[4:5], exec
	v_mbcnt_lo_u32_b32 v0, s4, 0
	v_mbcnt_hi_u32_b32 v0, s5, v0
	v_cmp_eq_u32_e32 vcc, 0, v0
	s_waitcnt vmcnt(0)
.LBB0_2434:
	s_waitcnt vmcnt(0)

.Lopt27_19:
.LBB0_2546:
	s_or_b64 exec, exec, s[4:5]
	s_mov_b64 s[4:5], exec
	v_mbcnt_lo_u32_b32 v0, s4, 0
	v_mbcnt_hi_u32_b32 v0, s5, v0
	v_cmp_eq_u32_e32 vcc, 0, v0
	s_waitcnt vmcnt(0)
.LBB0_2548:
	s_waitcnt vmcnt(0)
